# v18 + MLA: a fully masked key tile also skips its mask / softmax / rescale work for that wave (m unchanged, alpha = 1, row sum 0)
# speedup vs baseline: 1.0056x; 1.0013x over previous
.LBB0_944:
	s_sub_i32 s1, s37, 0x9e
	s_cmp_gt_i32 s1, s35
	s_cbranch_scc1 .Lmla_full1
	s_sub_i32 s1, s37, 64
	s_cmp_le_i32 s1, s35
	s_cbranch_scc1 .LBB0_946
	v_add_u32_e32 v98, 27, v229
	v_cmp_lt_i32_e32 vcc, -1, v98
	s_nop 1
	v_cndmask_b32_e32 v66, v216, v66, vcc
	v_cmp_lt_i32_e32 vcc, 31, v98
	v_add_u32_e32 v98, 26, v229
	s_nop 0
	v_cndmask_b32_e32 v82, v216, v82, vcc
	v_cmp_lt_i32_e32 vcc, -1, v98
	s_nop 1
	v_cndmask_b32_e32 v67, v216, v67, vcc
	v_cmp_lt_i32_e32 vcc, 31, v98
	v_add_u32_e32 v98, 25, v229
	s_nop 0
	v_cndmask_b32_e32 v83, v216, v83, vcc
	v_cmp_lt_i32_e32 vcc, -1, v98
	s_nop 1
	v_cndmask_b32_e32 v68, v216, v68, vcc
	v_cmp_lt_i32_e32 vcc, 31, v98
	v_add_u32_e32 v98, 24, v229
	s_nop 0
	v_cndmask_b32_e32 v84, v216, v84, vcc
	v_cmp_lt_i32_e32 vcc, -1, v98
	s_nop 1
	v_cndmask_b32_e32 v69, v216, v69, vcc
	v_cmp_lt_i32_e32 vcc, 31, v98
	v_add_u32_e32 v98, 19, v229
	s_nop 0
	v_cndmask_b32_e32 v85, v216, v85, vcc
	v_cmp_lt_i32_e32 vcc, -1, v98
	s_nop 1
	v_cndmask_b32_e32 v70, v216, v70, vcc
	v_cmp_lt_i32_e32 vcc, 31, v98
	v_add_u32_e32 v98, 18, v229
	s_nop 0
	v_cndmask_b32_e32 v86, v216, v86, vcc
	v_cmp_lt_i32_e32 vcc, -1, v98
	s_nop 1
	v_cndmask_b32_e32 v71, v216, v71, vcc
	v_cmp_lt_i32_e32 vcc, 31, v98
	v_add_u32_e32 v98, 17, v229
	s_nop 0
	v_cndmask_b32_e32 v87, v216, v87, vcc
	v_cmp_lt_i32_e32 vcc, -1, v98
	s_nop 1
	v_cndmask_b32_e32 v72, v216, v72, vcc
	v_cmp_lt_i32_e32 vcc, 31, v98
	v_add_u32_e32 v98, 16, v229
	s_nop 0
	v_cndmask_b32_e32 v88, v216, v88, vcc
	v_cmp_lt_i32_e32 vcc, -1, v98
	s_nop 1
	v_cndmask_b32_e32 v73, v216, v73, vcc
	v_cmp_lt_i32_e32 vcc, 31, v98
	v_add_u32_e32 v98, 11, v229
	s_nop 0
	v_cndmask_b32_e32 v89, v216, v89, vcc
	v_cmp_lt_i32_e32 vcc, -1, v98
	s_nop 1
	v_cndmask_b32_e32 v74, v216, v74, vcc
	v_cmp_lt_i32_e32 vcc, 31, v98
	v_add_u32_e32 v98, 10, v229
	s_nop 0
	v_cndmask_b32_e32 v90, v216, v90, vcc
	v_cmp_lt_i32_e32 vcc, -1, v98
	s_nop 1
	v_cndmask_b32_e32 v75, v216, v75, vcc
	v_cmp_lt_i32_e32 vcc, 31, v98
	v_add_u32_e32 v98, 9, v229
	s_nop 0
	v_cndmask_b32_e32 v91, v216, v91, vcc
	v_cmp_lt_i32_e32 vcc, -1, v98
	s_nop 1
	v_cndmask_b32_e32 v76, v216, v76, vcc
	v_cmp_lt_i32_e32 vcc, 31, v98
	v_add_u32_e32 v98, 8, v229
	s_nop 0
	v_cndmask_b32_e32 v92, v216, v92, vcc
	v_cmp_lt_i32_e32 vcc, -1, v98
	s_nop 1
	v_cndmask_b32_e32 v77, v216, v77, vcc
	v_cmp_lt_i32_e32 vcc, 31, v98
	v_add_u32_e32 v98, 3, v229
	s_nop 0
	v_cndmask_b32_e32 v93, v216, v93, vcc
	v_cmp_lt_i32_e32 vcc, -1, v98
	s_nop 1
	v_cndmask_b32_e32 v78, v216, v78, vcc
	v_cmp_lt_i32_e32 vcc, 31, v98
	v_add_u32_e32 v98, 2, v229
	s_nop 0
	v_cndmask_b32_e32 v94, v216, v94, vcc
	v_cmp_lt_i32_e32 vcc, -1, v98
	s_nop 1
	v_cndmask_b32_e32 v79, v216, v79, vcc
	v_cmp_lt_i32_e32 vcc, 31, v98
	v_add_u32_e32 v98, 1, v229
	s_nop 0
	v_cndmask_b32_e32 v95, v216, v95, vcc
	v_cmp_lt_i32_e32 vcc, -1, v98
	s_nop 1
	v_cndmask_b32_e32 v80, v216, v80, vcc
	v_cmp_lt_i32_e32 vcc, 31, v98
	s_nop 1
	v_cndmask_b32_e32 v96, v216, v96, vcc
	v_cmp_lt_i32_e32 vcc, -1, v229
	s_nop 1
	v_cndmask_b32_e32 v81, v216, v81, vcc
	v_cmp_lt_i32_e32 vcc, 31, v229
	s_nop 1
	v_cndmask_b32_e32 v97, v216, v97, vcc

.LBB0_952:
	s_sub_i32 s1, s37, 94
	s_cmp_gt_i32 s1, s35
	s_cbranch_scc1 .Lmla_full2
	s_cmp_le_i32 s37, s35
	s_cbranch_scc1 .LBB0_954
	v_subrev_u32_e32 v178, 37, v229
	v_cmp_lt_i32_e32 vcc, -1, v178
	s_nop 1
	v_cndmask_b32_e32 v114, v216, v114, vcc
	v_cmp_lt_i32_e32 vcc, 31, v178
	v_subrev_u32_e32 v178, 38, v229
	s_nop 0
	v_cndmask_b32_e32 v98, v216, v98, vcc
	v_cmp_lt_i32_e32 vcc, -1, v178
	s_nop 1
	v_cndmask_b32_e32 v115, v216, v115, vcc
	v_cmp_lt_i32_e32 vcc, 31, v178
	v_subrev_u32_e32 v178, 39, v229
	s_nop 0
	v_cndmask_b32_e32 v99, v216, v99, vcc
	v_cmp_lt_i32_e32 vcc, -1, v178
	s_nop 1
	v_cndmask_b32_e32 v116, v216, v116, vcc
	v_cmp_lt_i32_e32 vcc, 31, v178
	v_subrev_u32_e32 v178, 40, v229
	s_nop 0
	v_cndmask_b32_e32 v100, v216, v100, vcc
	v_cmp_lt_i32_e32 vcc, -1, v178
	s_nop 1
	v_cndmask_b32_e32 v117, v216, v117, vcc
	v_cmp_lt_i32_e32 vcc, 31, v178
	v_subrev_u32_e32 v178, 45, v229
	s_nop 0
	v_cndmask_b32_e32 v101, v216, v101, vcc
	v_cmp_lt_i32_e32 vcc, -1, v178
	s_nop 1
	v_cndmask_b32_e32 v118, v216, v118, vcc
	v_cmp_lt_i32_e32 vcc, 31, v178
	v_subrev_u32_e32 v178, 46, v229
	s_nop 0
	v_cndmask_b32_e32 v102, v216, v102, vcc
	v_cmp_lt_i32_e32 vcc, -1, v178
	s_nop 1
	v_cndmask_b32_e32 v119, v216, v119, vcc
	v_cmp_lt_i32_e32 vcc, 31, v178
	v_subrev_u32_e32 v178, 47, v229
	s_nop 0
	v_cndmask_b32_e32 v103, v216, v103, vcc
	v_cmp_lt_i32_e32 vcc, -1, v178
	s_nop 1
	v_cndmask_b32_e32 v120, v216, v120, vcc
	v_cmp_lt_i32_e32 vcc, 31, v178
	v_subrev_u32_e32 v178, 48, v229
	s_nop 0
	v_cndmask_b32_e32 v104, v216, v104, vcc
	v_cmp_lt_i32_e32 vcc, -1, v178
	s_nop 1
	v_cndmask_b32_e32 v121, v216, v121, vcc
	v_cmp_lt_i32_e32 vcc, 31, v178
	v_subrev_u32_e32 v178, 53, v229
	s_nop 0
	v_cndmask_b32_e32 v105, v216, v105, vcc
	v_cmp_lt_i32_e32 vcc, -1, v178
	s_nop 1
	v_cndmask_b32_e32 v122, v216, v122, vcc
	v_cmp_lt_i32_e32 vcc, 31, v178
	v_subrev_u32_e32 v178, 54, v229
	s_nop 0
	v_cndmask_b32_e32 v106, v216, v106, vcc
	v_cmp_lt_i32_e32 vcc, -1, v178
	s_nop 1
	v_cndmask_b32_e32 v123, v216, v123, vcc
	v_cmp_lt_i32_e32 vcc, 31, v178
	v_subrev_u32_e32 v178, 55, v229
	s_nop 0
	v_cndmask_b32_e32 v107, v216, v107, vcc
	v_cmp_lt_i32_e32 vcc, -1, v178
	s_nop 1
	v_cndmask_b32_e32 v124, v216, v124, vcc
	v_cmp_lt_i32_e32 vcc, 31, v178
	v_subrev_u32_e32 v178, 56, v229
	s_nop 0
	v_cndmask_b32_e32 v108, v216, v108, vcc
	v_cmp_lt_i32_e32 vcc, -1, v178
	s_nop 1
	v_cndmask_b32_e32 v125, v216, v125, vcc
	v_cmp_lt_i32_e32 vcc, 31, v178
	v_subrev_u32_e32 v178, 61, v229
	s_nop 0
	v_cndmask_b32_e32 v109, v216, v109, vcc
	v_cmp_lt_i32_e32 vcc, -1, v178
	s_nop 1
	v_cndmask_b32_e32 v126, v216, v126, vcc
	v_cmp_lt_i32_e32 vcc, 31, v178
	v_subrev_u32_e32 v178, 62, v229
	s_nop 0
	v_cndmask_b32_e32 v110, v216, v110, vcc
	v_cmp_lt_i32_e32 vcc, -1, v178
	s_nop 1
	v_cndmask_b32_e32 v127, v216, v127, vcc
	v_cmp_lt_i32_e32 vcc, 31, v178
	v_subrev_u32_e32 v178, 63, v229
	s_nop 0
	v_cndmask_b32_e32 v111, v216, v111, vcc
	v_cmp_lt_i32_e32 vcc, -1, v178
	s_nop 1
	v_cndmask_b32_e32 v128, v216, v128, vcc
	v_cmp_lt_i32_e32 vcc, 31, v178
	v_subrev_u32_e32 v178, 64, v229
	s_nop 0
	v_cndmask_b32_e32 v112, v216, v112, vcc
	v_cmp_lt_i32_e32 vcc, -1, v178
	s_nop 1
	v_cndmask_b32_e32 v129, v216, v129, vcc
	v_cmp_lt_i32_e32 vcc, 31, v178
	s_nop 1
	v_cndmask_b32_e32 v113, v216, v113, vcc

.Lmla_full1:
	s_lshl_b32 s50, s0, 14
	v_mov_b32_e32 v232, v231
	v_mov_b32_e32 v231, 1.0
	v_mov_b32_e32 v233, 0
	v_mov_b32_e32 v234, 0
	s_branch .Lmla_pvskip1
.Lmla_full2:
	v_add_f32_e32 v233, v233, v234
	v_fmac_f32_e32 v233, v230, v231
	v_mov_b32_e32 v230, v233
	v_mov_b32_e32 v231, v232
	v_mov_b32_e32 v234, 1.0
	s_branch .Lmla_pvskip2
